# out-projection and PEER query K loops: LDS-DMA pieces addressed as scalar base + lane offset too (on top of v18)
# speedup vs baseline: 1.0081x; 1.0037x over previous
.LBB0_1599:
	ds_read_b128 v[146:149], v164
	ds_read_b128 v[150:153], v164 offset:1024
	ds_read_b128 v[168:171], v164 offset:2048
	ds_read_b128 v[172:175], v164 offset:3072
	s_add_u32 s56, s54, 0xfff80080
	s_addc_u32 s57, s55, -1
	s_cmp_eq_u32 s82, 28
	s_cselect_b32 s59, s41, s57
	s_cselect_b32 s58, s78, s56
	s_cselect_b32 s57, s39, s81
	s_cselect_b32 s56, s79, s80
	s_add_i32 m0, s53, 0xc000
	ds_read_b128 v[176:179], v165
	ds_read_b128 v[180:183], v165 offset:1024
	ds_read_b128 v[184:187], v165 offset:2048
	ds_read_b128 v[188:191], v165 offset:3072
	ds_read_b128 v[192:195], v165 offset:4096
	ds_read_b128 v[196:199], v165 offset:5120
	ds_read_b128 v[200:203], v165 offset:6144
	ds_read_b128 v[204:207], v165 offset:7168
	global_load_lds_dwordx4 v138, s[54:55]
	s_add_i32 m0, s53, 0xe000
	s_nop 0
	global_load_lds_dwordx4 v140, s[54:55]
	s_waitcnt lgkmcnt(8)
	s_barrier
	s_waitcnt lgkmcnt(0)
	s_setprio 1
	s_waitcnt lgkmcnt(0)
	v_mfma_i32_16x16x64_i8 v[126:129], v[146:149], v[176:179], v[126:129]
	v_mfma_i32_16x16x64_i8 v[122:125], v[168:171], v[176:179], v[122:125]
	v_mfma_i32_16x16x64_i8 v[110:113], v[146:149], v[184:187], v[110:113]
	v_mfma_i32_16x16x64_i8 v[106:109], v[168:171], v[184:187], v[106:109]
	v_mfma_i32_16x16x64_i8 v[94:97], v[146:149], v[192:195], v[94:97]
	v_mfma_i32_16x16x64_i8 v[90:93], v[168:171], v[192:195], v[90:93]
	v_mfma_i32_16x16x64_i8 v[78:81], v[146:149], v[200:203], v[78:81]
	v_mfma_i32_16x16x64_i8 v[74:77], v[168:171], v[200:203], v[74:77]
	v_mfma_i32_16x16x64_i8 v[126:129], v[150:153], v[180:183], v[126:129]
	v_mfma_i32_16x16x64_i8 v[122:125], v[172:175], v[180:183], v[122:125]
	v_mfma_i32_16x16x64_i8 v[110:113], v[150:153], v[188:191], v[110:113]
	v_mfma_i32_16x16x64_i8 v[106:109], v[172:175], v[188:191], v[106:109]
	v_mfma_i32_16x16x64_i8 v[94:97], v[150:153], v[196:199], v[94:97]
	v_mfma_i32_16x16x64_i8 v[90:93], v[172:175], v[196:199], v[90:93]
	v_mfma_i32_16x16x64_i8 v[78:81], v[150:153], v[204:207], v[78:81]
	v_mfma_i32_16x16x64_i8 v[74:77], v[172:175], v[204:207], v[74:77]
	s_setprio 0
	s_barrier
	s_add_i32 s83, s71, s64
	s_add_u32 s100, s56, 0x80
	s_addc_u32 s101, s57, 0
	s_mov_b32 m0, s83
	ds_read_b128 v[208:211], v166
	ds_read_b128 v[212:215], v166 offset:1024
	ds_read_b128 v[216:219], v166 offset:2048
	ds_read_b128 v[220:223], v166 offset:3072
	global_load_lds_dwordx4 v132, s[56:57]
	s_add_i32 m0, s83, 0x2000
	s_nop 0
	global_load_lds_dwordx4 v136, s[56:57]
	s_barrier
	s_waitcnt lgkmcnt(0)
	s_setprio 1
	s_waitcnt lgkmcnt(0)
	v_mfma_i32_16x16x64_i8 v[118:121], v[208:211], v[176:179], v[118:121]
	v_mfma_i32_16x16x64_i8 v[114:117], v[216:219], v[176:179], v[114:117]
	v_mfma_i32_16x16x64_i8 v[102:105], v[208:211], v[184:187], v[102:105]
	v_mfma_i32_16x16x64_i8 v[98:101], v[216:219], v[184:187], v[98:101]
	v_mfma_i32_16x16x64_i8 v[86:89], v[208:211], v[192:195], v[86:89]
	v_mfma_i32_16x16x64_i8 v[82:85], v[216:219], v[192:195], v[82:85]
	v_mfma_i32_16x16x64_i8 v[70:73], v[208:211], v[200:203], v[70:73]
	v_mfma_i32_16x16x64_i8 v[66:69], v[216:219], v[200:203], v[66:69]
	v_mfma_i32_16x16x64_i8 v[118:121], v[212:215], v[180:183], v[118:121]
	v_mfma_i32_16x16x64_i8 v[114:117], v[220:223], v[180:183], v[114:117]
	v_mfma_i32_16x16x64_i8 v[102:105], v[212:215], v[188:191], v[102:105]
	v_mfma_i32_16x16x64_i8 v[98:101], v[220:223], v[188:191], v[98:101]
	v_mfma_i32_16x16x64_i8 v[86:89], v[212:215], v[196:199], v[86:89]
	v_mfma_i32_16x16x64_i8 v[82:85], v[220:223], v[196:199], v[82:85]
	v_mfma_i32_16x16x64_i8 v[70:73], v[212:215], v[204:207], v[70:73]
	v_mfma_i32_16x16x64_i8 v[66:69], v[220:223], v[204:207], v[66:69]
	s_setprio 0
	s_mov_b32 m0, s53
	s_add_u32 s98, s58, 0x80
	s_addc_u32 s99, s59, 0
	s_barrier
	ds_read_b128 v[176:179], v165 offset:16384
	ds_read_b128 v[180:183], v165 offset:17408
	ds_read_b128 v[184:187], v165 offset:18432
	ds_read_b128 v[188:191], v165 offset:19456
	ds_read_b128 v[192:195], v165 offset:20480
	ds_read_b128 v[196:199], v165 offset:21504
	ds_read_b128 v[200:203], v165 offset:22528
	ds_read_b128 v[204:207], v165 offset:23552
	global_load_lds_dwordx4 v130, s[58:59]
	s_mov_b32 m0, s65
	s_nop 0
	global_load_lds_dwordx4 v134, s[58:59]
	s_barrier
	s_waitcnt lgkmcnt(0)
	s_setprio 1
	s_waitcnt lgkmcnt(0)
	v_mfma_i32_16x16x64_i8 v[62:65], v[146:149], v[176:179], v[62:65]
	v_mfma_i32_16x16x64_i8 v[58:61], v[168:171], v[176:179], v[58:61]
	v_mfma_i32_16x16x64_i8 v[46:49], v[146:149], v[184:187], v[46:49]
	v_mfma_i32_16x16x64_i8 v[42:45], v[168:171], v[184:187], v[42:45]
	v_mfma_i32_16x16x64_i8 v[30:33], v[146:149], v[192:195], v[30:33]
	v_mfma_i32_16x16x64_i8 v[26:29], v[168:171], v[192:195], v[26:29]
	v_mfma_i32_16x16x64_i8 v[14:17], v[146:149], v[200:203], v[14:17]
	v_mfma_i32_16x16x64_i8 v[10:13], v[168:171], v[200:203], v[10:13]
	v_mfma_i32_16x16x64_i8 v[62:65], v[150:153], v[180:183], v[62:65]
	v_mfma_i32_16x16x64_i8 v[58:61], v[172:175], v[180:183], v[58:61]
	v_mfma_i32_16x16x64_i8 v[46:49], v[150:153], v[188:191], v[46:49]
	v_mfma_i32_16x16x64_i8 v[42:45], v[172:175], v[188:191], v[42:45]
	v_mfma_i32_16x16x64_i8 v[30:33], v[150:153], v[196:199], v[30:33]
	v_mfma_i32_16x16x64_i8 v[26:29], v[172:175], v[196:199], v[26:29]
	v_mfma_i32_16x16x64_i8 v[14:17], v[150:153], v[204:207], v[14:17]
	v_mfma_i32_16x16x64_i8 v[10:13], v[172:175], v[204:207], v[10:13]
	s_setprio 0
	s_barrier
	s_add_u32 s86, s56, 0x80000
	s_addc_u32 s87, s57, 0
	s_add_i32 s83, s72, s64
	s_mov_b32 m0, s83
	s_nop 0
	global_load_lds_dwordx4 v132, s[86:87]
	s_add_i32 m0, s83, 0x2000
	s_nop 0
	global_load_lds_dwordx4 v136, s[86:87]
	s_waitcnt vmcnt(6)
	s_barrier
	s_setprio 1
	v_mfma_i32_16x16x64_i8 v[54:57], v[208:211], v[176:179], v[54:57]
	v_mfma_i32_16x16x64_i8 v[50:53], v[216:219], v[176:179], v[50:53]
	v_mfma_i32_16x16x64_i8 v[38:41], v[208:211], v[184:187], v[38:41]
	v_mfma_i32_16x16x64_i8 v[34:37], v[216:219], v[184:187], v[34:37]
	v_mfma_i32_16x16x64_i8 v[22:25], v[208:211], v[192:195], v[22:25]
	v_mfma_i32_16x16x64_i8 v[18:21], v[216:219], v[192:195], v[18:21]
	v_mfma_i32_16x16x64_i8 v[6:9], v[208:211], v[200:203], v[6:9]
	v_mfma_i32_16x16x64_i8 v[2:5], v[216:219], v[200:203], v[2:5]
	v_mfma_i32_16x16x64_i8 v[54:57], v[212:215], v[180:183], v[54:57]
	v_mfma_i32_16x16x64_i8 v[50:53], v[220:223], v[180:183], v[50:53]
	v_mfma_i32_16x16x64_i8 v[38:41], v[212:215], v[188:191], v[38:41]
	v_mfma_i32_16x16x64_i8 v[34:37], v[220:223], v[188:191], v[34:37]
	v_mfma_i32_16x16x64_i8 v[22:25], v[212:215], v[196:199], v[22:25]
	v_mfma_i32_16x16x64_i8 v[18:21], v[220:223], v[196:199], v[18:21]
	v_mfma_i32_16x16x64_i8 v[6:9], v[212:215], v[204:207], v[6:9]
	v_mfma_i32_16x16x64_i8 v[2:5], v[220:223], v[204:207], v[2:5]
	s_setprio 0
	s_add_i32 s83, 0, 0x18000
	v_add_u32_e32 v167, s83, v162
	s_barrier
	ds_read_b128 v[146:149], v167
	ds_read_b128 v[150:153], v167 offset:1024
	ds_read_b128 v[168:171], v167 offset:2048
	ds_read_b128 v[172:175], v167 offset:3072
	s_add_u32 s58, s58, 0x80000
	s_addc_u32 s59, s59, 0
	s_mov_b32 m0, s66
	ds_read_b128 v[176:179], v165 offset:32768
	ds_read_b128 v[180:183], v165 offset:33792
	ds_read_b128 v[184:187], v165 offset:34816
	ds_read_b128 v[188:191], v165 offset:35840
	ds_read_b128 v[192:195], v165 offset:36864
	ds_read_b128 v[196:199], v165 offset:37888
	ds_read_b128 v[200:203], v165 offset:38912
	ds_read_b128 v[204:207], v165 offset:39936
	global_load_lds_dwordx4 v130, s[58:59]
	s_mov_b32 m0, s67
	s_nop 0
	global_load_lds_dwordx4 v134, s[58:59]
	s_waitcnt lgkmcnt(8)
	s_barrier
	s_waitcnt lgkmcnt(0)
	s_setprio 1
	s_waitcnt lgkmcnt(0)
	v_mfma_i32_16x16x64_i8 v[126:129], v[146:149], v[176:179], v[126:129]
	v_mfma_i32_16x16x64_i8 v[122:125], v[168:171], v[176:179], v[122:125]
	v_mfma_i32_16x16x64_i8 v[110:113], v[146:149], v[184:187], v[110:113]
	v_mfma_i32_16x16x64_i8 v[106:109], v[168:171], v[184:187], v[106:109]
	v_mfma_i32_16x16x64_i8 v[94:97], v[146:149], v[192:195], v[94:97]
	v_mfma_i32_16x16x64_i8 v[90:93], v[168:171], v[192:195], v[90:93]
	v_mfma_i32_16x16x64_i8 v[78:81], v[146:149], v[200:203], v[78:81]
	v_mfma_i32_16x16x64_i8 v[74:77], v[168:171], v[200:203], v[74:77]
	v_mfma_i32_16x16x64_i8 v[126:129], v[150:153], v[180:183], v[126:129]
	v_mfma_i32_16x16x64_i8 v[122:125], v[172:175], v[180:183], v[122:125]
	v_mfma_i32_16x16x64_i8 v[110:113], v[150:153], v[188:191], v[110:113]
	v_mfma_i32_16x16x64_i8 v[106:109], v[172:175], v[188:191], v[106:109]
	v_mfma_i32_16x16x64_i8 v[94:97], v[150:153], v[196:199], v[94:97]
	v_mfma_i32_16x16x64_i8 v[90:93], v[172:175], v[196:199], v[90:93]
	v_mfma_i32_16x16x64_i8 v[78:81], v[150:153], v[204:207], v[78:81]
	v_mfma_i32_16x16x64_i8 v[74:77], v[172:175], v[204:207], v[74:77]
	s_setprio 0
	s_barrier
	s_add_i32 s58, 0, 0x1c000
	s_add_i32 s59, s83, s64
	v_add_u32_e32 v167, s58, v162
	s_mov_b32 m0, s59
	ds_read_b128 v[208:211], v167
	ds_read_b128 v[212:215], v167 offset:1024
	ds_read_b128 v[216:219], v167 offset:2048
	ds_read_b128 v[220:223], v167 offset:3072
	global_load_lds_dwordx4 v132, s[100:101]
	s_add_i32 m0, s59, 0x2000
	s_nop 0
	global_load_lds_dwordx4 v136, s[100:101]
	s_barrier
	s_waitcnt lgkmcnt(0)
	s_setprio 1
	s_waitcnt lgkmcnt(0)
	v_mfma_i32_16x16x64_i8 v[118:121], v[208:211], v[176:179], v[118:121]
	v_mfma_i32_16x16x64_i8 v[114:117], v[216:219], v[176:179], v[114:117]
	v_mfma_i32_16x16x64_i8 v[102:105], v[208:211], v[184:187], v[102:105]
	v_mfma_i32_16x16x64_i8 v[98:101], v[216:219], v[184:187], v[98:101]
	v_mfma_i32_16x16x64_i8 v[86:89], v[208:211], v[192:195], v[86:89]
	v_mfma_i32_16x16x64_i8 v[82:85], v[216:219], v[192:195], v[82:85]
	v_mfma_i32_16x16x64_i8 v[70:73], v[208:211], v[200:203], v[70:73]
	v_mfma_i32_16x16x64_i8 v[66:69], v[216:219], v[200:203], v[66:69]
	v_mfma_i32_16x16x64_i8 v[118:121], v[212:215], v[180:183], v[118:121]
	v_mfma_i32_16x16x64_i8 v[114:117], v[220:223], v[180:183], v[114:117]
	v_mfma_i32_16x16x64_i8 v[102:105], v[212:215], v[188:191], v[102:105]
	v_mfma_i32_16x16x64_i8 v[98:101], v[220:223], v[188:191], v[98:101]
	v_mfma_i32_16x16x64_i8 v[86:89], v[212:215], v[196:199], v[86:89]
	v_mfma_i32_16x16x64_i8 v[82:85], v[220:223], v[196:199], v[82:85]
	v_mfma_i32_16x16x64_i8 v[70:73], v[212:215], v[204:207], v[70:73]
	v_mfma_i32_16x16x64_i8 v[66:69], v[220:223], v[204:207], v[66:69]
	s_setprio 0
	s_mov_b32 m0, s69
	s_barrier
	ds_read_b128 v[176:179], v165 offset:49152
	ds_read_b128 v[180:183], v165 offset:50176
	ds_read_b128 v[184:187], v165 offset:51200
	ds_read_b128 v[188:191], v165 offset:52224
	ds_read_b128 v[192:195], v165 offset:53248
	ds_read_b128 v[196:199], v165 offset:54272
	ds_read_b128 v[200:203], v165 offset:55296
	ds_read_b128 v[204:207], v165 offset:56320
	global_load_lds_dwordx4 v130, s[98:99]
	s_mov_b32 m0, s70
	s_nop 0
	global_load_lds_dwordx4 v134, s[98:99]
	s_barrier
	s_waitcnt lgkmcnt(0)
	s_setprio 1
	s_waitcnt lgkmcnt(0)
	v_mfma_i32_16x16x64_i8 v[62:65], v[146:149], v[176:179], v[62:65]
	v_mfma_i32_16x16x64_i8 v[58:61], v[168:171], v[176:179], v[58:61]
	v_mfma_i32_16x16x64_i8 v[46:49], v[146:149], v[184:187], v[46:49]
	v_mfma_i32_16x16x64_i8 v[42:45], v[168:171], v[184:187], v[42:45]
	v_mfma_i32_16x16x64_i8 v[30:33], v[146:149], v[192:195], v[30:33]
	v_mfma_i32_16x16x64_i8 v[26:29], v[168:171], v[192:195], v[26:29]
	v_mfma_i32_16x16x64_i8 v[14:17], v[146:149], v[200:203], v[14:17]
	v_mfma_i32_16x16x64_i8 v[10:13], v[168:171], v[200:203], v[10:13]
	v_mfma_i32_16x16x64_i8 v[62:65], v[150:153], v[180:183], v[62:65]
	v_mfma_i32_16x16x64_i8 v[58:61], v[172:175], v[180:183], v[58:61]
	v_mfma_i32_16x16x64_i8 v[46:49], v[150:153], v[188:191], v[46:49]
	v_mfma_i32_16x16x64_i8 v[42:45], v[172:175], v[188:191], v[42:45]
	v_mfma_i32_16x16x64_i8 v[30:33], v[150:153], v[196:199], v[30:33]
	v_mfma_i32_16x16x64_i8 v[26:29], v[172:175], v[196:199], v[26:29]
	v_mfma_i32_16x16x64_i8 v[14:17], v[150:153], v[204:207], v[14:17]
	v_mfma_i32_16x16x64_i8 v[10:13], v[172:175], v[204:207], v[10:13]
	s_setprio 0
	s_barrier
	s_add_u32 s56, s56, 0x80080
	s_addc_u32 s57, s57, 0
	s_add_i32 s58, s58, s64
	s_mov_b32 m0, s58
	s_nop 0
	global_load_lds_dwordx4 v132, s[56:57]
	s_add_i32 m0, s58, 0x2000
	s_nop 0
	global_load_lds_dwordx4 v136, s[56:57]
	s_waitcnt vmcnt(6)
	s_barrier
	s_setprio 1
	v_mfma_i32_16x16x64_i8 v[54:57], v[208:211], v[176:179], v[54:57]
	v_mfma_i32_16x16x64_i8 v[50:53], v[216:219], v[176:179], v[50:53]
	v_mfma_i32_16x16x64_i8 v[38:41], v[208:211], v[184:187], v[38:41]
	v_mfma_i32_16x16x64_i8 v[34:37], v[216:219], v[184:187], v[34:37]
	v_mfma_i32_16x16x64_i8 v[22:25], v[208:211], v[192:195], v[22:25]
	v_mfma_i32_16x16x64_i8 v[18:21], v[216:219], v[192:195], v[18:21]
	v_mfma_i32_16x16x64_i8 v[6:9], v[208:211], v[200:203], v[6:9]
	v_mfma_i32_16x16x64_i8 v[2:5], v[216:219], v[200:203], v[2:5]
	v_mfma_i32_16x16x64_i8 v[54:57], v[212:215], v[180:183], v[54:57]
	v_mfma_i32_16x16x64_i8 v[50:53], v[220:223], v[180:183], v[50:53]
	v_mfma_i32_16x16x64_i8 v[38:41], v[212:215], v[188:191], v[38:41]
	v_mfma_i32_16x16x64_i8 v[34:37], v[220:223], v[188:191], v[34:37]
	v_mfma_i32_16x16x64_i8 v[22:25], v[212:215], v[196:199], v[22:25]
	v_mfma_i32_16x16x64_i8 v[18:21], v[220:223], v[196:199], v[18:21]
	v_mfma_i32_16x16x64_i8 v[6:9], v[212:215], v[204:207], v[6:9]
	v_mfma_i32_16x16x64_i8 v[2:5], v[220:223], v[204:207], v[2:5]
	s_setprio 0
	s_add_i32 s82, s82, 2
	s_add_u32 s54, s54, 0x100
	s_addc_u32 s55, s55, 0
	s_add_u32 s80, s80, 0x100
	s_addc_u32 s81, s81, 0
	s_cmp_gt_u32 s82, 29
	s_barrier
	s_cbranch_scc0 .LBB0_1599
	s_and_b64 vcc, exec, s[20:21]
	s_cbranch_vccz .LBB0_1602
	s_barrier

.LBB0_1744:
	ds_read_b128 v[162:165], v151
	ds_read_b128 v[166:169], v151 offset:1024
	ds_read_b128 v[170:173], v151 offset:2048
	ds_read_b128 v[174:177], v151 offset:3072
	s_add_u32 s40, s38, 0xfff00080
	s_addc_u32 s41, s39, -1
	s_cmp_eq_u32 s71, 60
	s_cselect_b32 s43, s29, s41
	s_cselect_b32 s42, s67, s40
	s_cselect_b32 s41, s27, s70
	s_cselect_b32 s40, s68, s69
	s_add_i32 m0, s37, 0xc000
	ds_read_b128 v[178:181], v152
	ds_read_b128 v[182:185], v152 offset:1024
	ds_read_b128 v[186:189], v152 offset:2048
	ds_read_b128 v[190:193], v152 offset:3072
	ds_read_b128 v[194:197], v152 offset:4096
	ds_read_b128 v[198:201], v152 offset:5120
	ds_read_b128 v[202:205], v152 offset:6144
	ds_read_b128 v[206:209], v152 offset:7168
	global_load_lds_dwordx4 v138, s[38:39]
	s_add_i32 m0, s37, 0xe000
	s_nop 0
	global_load_lds_dwordx4 v140, s[38:39]
	s_waitcnt lgkmcnt(8)
	s_barrier
	s_waitcnt lgkmcnt(0)
	s_setprio 1
	s_waitcnt lgkmcnt(0)
	v_mfma_f32_16x16x32_bf16 v[126:129], v[162:165], v[178:181], v[126:129]
	v_mfma_f32_16x16x32_bf16 v[122:125], v[170:173], v[178:181], v[122:125]
	v_mfma_f32_16x16x32_bf16 v[110:113], v[162:165], v[186:189], v[110:113]
	v_mfma_f32_16x16x32_bf16 v[106:109], v[170:173], v[186:189], v[106:109]
	v_mfma_f32_16x16x32_bf16 v[94:97], v[162:165], v[194:197], v[94:97]
	v_mfma_f32_16x16x32_bf16 v[90:93], v[170:173], v[194:197], v[90:93]
	v_mfma_f32_16x16x32_bf16 v[78:81], v[162:165], v[202:205], v[78:81]
	v_mfma_f32_16x16x32_bf16 v[74:77], v[170:173], v[202:205], v[74:77]
	v_mfma_f32_16x16x32_bf16 v[126:129], v[166:169], v[182:185], v[126:129]
	v_mfma_f32_16x16x32_bf16 v[122:125], v[174:177], v[182:185], v[122:125]
	v_mfma_f32_16x16x32_bf16 v[110:113], v[166:169], v[190:193], v[110:113]
	v_mfma_f32_16x16x32_bf16 v[106:109], v[174:177], v[190:193], v[106:109]
	v_mfma_f32_16x16x32_bf16 v[94:97], v[166:169], v[198:201], v[94:97]
	v_mfma_f32_16x16x32_bf16 v[90:93], v[174:177], v[198:201], v[90:93]
	v_mfma_f32_16x16x32_bf16 v[78:81], v[166:169], v[206:209], v[78:81]
	v_mfma_f32_16x16x32_bf16 v[74:77], v[174:177], v[206:209], v[74:77]
	s_setprio 0
	s_barrier
	s_add_i32 s72, s47, s54
	s_add_u32 s100, s40, 0x80
	s_addc_u32 s101, s41, 0
	s_mov_b32 m0, s72
	ds_read_b128 v[210:213], v153
	ds_read_b128 v[214:217], v153 offset:1024
	ds_read_b128 v[218:221], v153 offset:2048
	ds_read_b128 v[222:225], v153 offset:3072
	global_load_lds_dwordx4 v132, s[40:41]
	s_add_i32 m0, s72, 0x2000
	s_nop 0
	global_load_lds_dwordx4 v136, s[40:41]
	s_barrier
	s_waitcnt lgkmcnt(0)
	s_setprio 1
	s_waitcnt lgkmcnt(0)
	v_mfma_f32_16x16x32_bf16 v[118:121], v[210:213], v[178:181], v[118:121]
	v_mfma_f32_16x16x32_bf16 v[114:117], v[218:221], v[178:181], v[114:117]
	v_mfma_f32_16x16x32_bf16 v[102:105], v[210:213], v[186:189], v[102:105]
	v_mfma_f32_16x16x32_bf16 v[98:101], v[218:221], v[186:189], v[98:101]
	v_mfma_f32_16x16x32_bf16 v[86:89], v[210:213], v[194:197], v[86:89]
	v_mfma_f32_16x16x32_bf16 v[82:85], v[218:221], v[194:197], v[82:85]
	v_mfma_f32_16x16x32_bf16 v[70:73], v[210:213], v[202:205], v[70:73]
	v_mfma_f32_16x16x32_bf16 v[66:69], v[218:221], v[202:205], v[66:69]
	v_mfma_f32_16x16x32_bf16 v[118:121], v[214:217], v[182:185], v[118:121]
	v_mfma_f32_16x16x32_bf16 v[114:117], v[222:225], v[182:185], v[114:117]
	v_mfma_f32_16x16x32_bf16 v[102:105], v[214:217], v[190:193], v[102:105]
	v_mfma_f32_16x16x32_bf16 v[98:101], v[222:225], v[190:193], v[98:101]
	v_mfma_f32_16x16x32_bf16 v[86:89], v[214:217], v[198:201], v[86:89]
	v_mfma_f32_16x16x32_bf16 v[82:85], v[222:225], v[198:201], v[82:85]
	v_mfma_f32_16x16x32_bf16 v[70:73], v[214:217], v[206:209], v[70:73]
	v_mfma_f32_16x16x32_bf16 v[66:69], v[222:225], v[206:209], v[66:69]
	s_setprio 0
	s_mov_b32 m0, s37
	s_add_u32 s98, s42, 0x80
	s_addc_u32 s99, s43, 0
	s_barrier
	ds_read_b128 v[178:181], v152 offset:16384
	ds_read_b128 v[182:185], v152 offset:17408
	ds_read_b128 v[186:189], v152 offset:18432
	ds_read_b128 v[190:193], v152 offset:19456
	ds_read_b128 v[194:197], v152 offset:20480
	ds_read_b128 v[198:201], v152 offset:21504
	ds_read_b128 v[202:205], v152 offset:22528
	ds_read_b128 v[206:209], v152 offset:23552
	global_load_lds_dwordx4 v130, s[42:43]
	s_mov_b32 m0, s55
	s_nop 0
	global_load_lds_dwordx4 v134, s[42:43]
	s_barrier
	s_waitcnt lgkmcnt(0)
	s_setprio 1
	s_waitcnt lgkmcnt(0)
	v_mfma_f32_16x16x32_bf16 v[62:65], v[162:165], v[178:181], v[62:65]
	v_mfma_f32_16x16x32_bf16 v[58:61], v[170:173], v[178:181], v[58:61]
	v_mfma_f32_16x16x32_bf16 v[50:53], v[162:165], v[186:189], v[50:53]
	v_mfma_f32_16x16x32_bf16 v[42:45], v[170:173], v[186:189], v[42:45]
	v_mfma_f32_16x16x32_bf16 v[34:37], v[162:165], v[194:197], v[34:37]
	v_mfma_f32_16x16x32_bf16 v[26:29], v[170:173], v[194:197], v[26:29]
	v_mfma_f32_16x16x32_bf16 v[18:21], v[162:165], v[202:205], v[18:21]
	v_mfma_f32_16x16x32_bf16 v[10:13], v[170:173], v[202:205], v[10:13]
	v_mfma_f32_16x16x32_bf16 v[62:65], v[166:169], v[182:185], v[62:65]
	v_mfma_f32_16x16x32_bf16 v[58:61], v[174:177], v[182:185], v[58:61]
	v_mfma_f32_16x16x32_bf16 v[50:53], v[166:169], v[190:193], v[50:53]
	v_mfma_f32_16x16x32_bf16 v[42:45], v[174:177], v[190:193], v[42:45]
	v_mfma_f32_16x16x32_bf16 v[34:37], v[166:169], v[198:201], v[34:37]
	v_mfma_f32_16x16x32_bf16 v[26:29], v[174:177], v[198:201], v[26:29]
	v_mfma_f32_16x16x32_bf16 v[18:21], v[166:169], v[206:209], v[18:21]
	v_mfma_f32_16x16x32_bf16 v[10:13], v[174:177], v[206:209], v[10:13]
	s_setprio 0
	s_barrier
	s_add_u32 s72, s40, 0x100000
	s_addc_u32 s73, s41, 0
	s_add_i32 s74, s61, s54
	s_mov_b32 m0, s74
	s_nop 0
	global_load_lds_dwordx4 v132, s[72:73]
	s_add_i32 m0, s74, 0x2000
	s_nop 0
	global_load_lds_dwordx4 v136, s[72:73]
	s_waitcnt vmcnt(6)
	s_barrier
	s_setprio 1
	v_mfma_f32_16x16x32_bf16 v[54:57], v[210:213], v[178:181], v[54:57]
	v_mfma_f32_16x16x32_bf16 v[46:49], v[218:221], v[178:181], v[46:49]
	v_mfma_f32_16x16x32_bf16 v[38:41], v[210:213], v[186:189], v[38:41]
	v_mfma_f32_16x16x32_bf16 v[30:33], v[218:221], v[186:189], v[30:33]
	v_mfma_f32_16x16x32_bf16 v[22:25], v[210:213], v[194:197], v[22:25]
	v_mfma_f32_16x16x32_bf16 v[14:17], v[218:221], v[194:197], v[14:17]
	v_mfma_f32_16x16x32_bf16 v[6:9], v[210:213], v[202:205], v[6:9]
	v_mfma_f32_16x16x32_bf16 v[2:5], v[218:221], v[202:205], v[2:5]
	v_mfma_f32_16x16x32_bf16 v[54:57], v[214:217], v[182:185], v[54:57]
	v_mfma_f32_16x16x32_bf16 v[46:49], v[222:225], v[182:185], v[46:49]
	v_mfma_f32_16x16x32_bf16 v[38:41], v[214:217], v[190:193], v[38:41]
	v_mfma_f32_16x16x32_bf16 v[30:33], v[222:225], v[190:193], v[30:33]
	v_mfma_f32_16x16x32_bf16 v[22:25], v[214:217], v[198:201], v[22:25]
	v_mfma_f32_16x16x32_bf16 v[14:17], v[222:225], v[198:201], v[14:17]
	v_mfma_f32_16x16x32_bf16 v[6:9], v[214:217], v[206:209], v[6:9]
	v_mfma_f32_16x16x32_bf16 v[2:5], v[222:225], v[206:209], v[2:5]
	s_setprio 0
	s_add_i32 s72, 0, 0x18000
	v_add_u32_e32 v161, s72, v149
	s_barrier
	ds_read_b128 v[162:165], v161
	ds_read_b128 v[166:169], v161 offset:1024
	ds_read_b128 v[170:173], v161 offset:2048
	ds_read_b128 v[174:177], v161 offset:3072
	s_add_u32 s42, s42, 0x100000
	s_addc_u32 s43, s43, 0
	s_mov_b32 m0, s56
	ds_read_b128 v[178:181], v152 offset:32768
	ds_read_b128 v[182:185], v152 offset:33792
	ds_read_b128 v[186:189], v152 offset:34816
	ds_read_b128 v[190:193], v152 offset:35840
	ds_read_b128 v[194:197], v152 offset:36864
	ds_read_b128 v[198:201], v152 offset:37888
	ds_read_b128 v[202:205], v152 offset:38912
	ds_read_b128 v[206:209], v152 offset:39936
	global_load_lds_dwordx4 v130, s[42:43]
	s_mov_b32 m0, s57
	s_nop 0
	global_load_lds_dwordx4 v134, s[42:43]
	s_waitcnt lgkmcnt(8)
	s_barrier
	s_waitcnt lgkmcnt(0)
	s_setprio 1
	s_waitcnt lgkmcnt(0)
	v_mfma_f32_16x16x32_bf16 v[126:129], v[162:165], v[178:181], v[126:129]
	v_mfma_f32_16x16x32_bf16 v[122:125], v[170:173], v[178:181], v[122:125]
	v_mfma_f32_16x16x32_bf16 v[110:113], v[162:165], v[186:189], v[110:113]
	v_mfma_f32_16x16x32_bf16 v[106:109], v[170:173], v[186:189], v[106:109]
	v_mfma_f32_16x16x32_bf16 v[94:97], v[162:165], v[194:197], v[94:97]
	v_mfma_f32_16x16x32_bf16 v[90:93], v[170:173], v[194:197], v[90:93]
	v_mfma_f32_16x16x32_bf16 v[78:81], v[162:165], v[202:205], v[78:81]
	v_mfma_f32_16x16x32_bf16 v[74:77], v[170:173], v[202:205], v[74:77]
	v_mfma_f32_16x16x32_bf16 v[126:129], v[166:169], v[182:185], v[126:129]
	v_mfma_f32_16x16x32_bf16 v[122:125], v[174:177], v[182:185], v[122:125]
	v_mfma_f32_16x16x32_bf16 v[110:113], v[166:169], v[190:193], v[110:113]
	v_mfma_f32_16x16x32_bf16 v[106:109], v[174:177], v[190:193], v[106:109]
	v_mfma_f32_16x16x32_bf16 v[94:97], v[166:169], v[198:201], v[94:97]
	v_mfma_f32_16x16x32_bf16 v[90:93], v[174:177], v[198:201], v[90:93]
	v_mfma_f32_16x16x32_bf16 v[78:81], v[166:169], v[206:209], v[78:81]
	v_mfma_f32_16x16x32_bf16 v[74:77], v[174:177], v[206:209], v[74:77]
	s_setprio 0
	s_barrier
	s_add_i32 s42, 0, 0x1c000
	s_add_i32 s43, s72, s54
	v_add_u32_e32 v161, s42, v149
	s_mov_b32 m0, s43
	ds_read_b128 v[210:213], v161
	ds_read_b128 v[214:217], v161 offset:1024
	ds_read_b128 v[218:221], v161 offset:2048
	ds_read_b128 v[222:225], v161 offset:3072
	global_load_lds_dwordx4 v132, s[100:101]
	s_add_i32 m0, s43, 0x2000
	s_nop 0
	global_load_lds_dwordx4 v136, s[100:101]
	s_barrier
	s_waitcnt lgkmcnt(0)
	s_setprio 1
	s_waitcnt lgkmcnt(0)
	v_mfma_f32_16x16x32_bf16 v[118:121], v[210:213], v[178:181], v[118:121]
	v_mfma_f32_16x16x32_bf16 v[114:117], v[218:221], v[178:181], v[114:117]
	v_mfma_f32_16x16x32_bf16 v[102:105], v[210:213], v[186:189], v[102:105]
	v_mfma_f32_16x16x32_bf16 v[98:101], v[218:221], v[186:189], v[98:101]
	v_mfma_f32_16x16x32_bf16 v[86:89], v[210:213], v[194:197], v[86:89]
	v_mfma_f32_16x16x32_bf16 v[82:85], v[218:221], v[194:197], v[82:85]
	v_mfma_f32_16x16x32_bf16 v[70:73], v[210:213], v[202:205], v[70:73]
	v_mfma_f32_16x16x32_bf16 v[66:69], v[218:221], v[202:205], v[66:69]
	v_mfma_f32_16x16x32_bf16 v[118:121], v[214:217], v[182:185], v[118:121]
	v_mfma_f32_16x16x32_bf16 v[114:117], v[222:225], v[182:185], v[114:117]
	v_mfma_f32_16x16x32_bf16 v[102:105], v[214:217], v[190:193], v[102:105]
	v_mfma_f32_16x16x32_bf16 v[98:101], v[222:225], v[190:193], v[98:101]
	v_mfma_f32_16x16x32_bf16 v[86:89], v[214:217], v[198:201], v[86:89]
	v_mfma_f32_16x16x32_bf16 v[82:85], v[222:225], v[198:201], v[82:85]
	v_mfma_f32_16x16x32_bf16 v[70:73], v[214:217], v[206:209], v[70:73]
	v_mfma_f32_16x16x32_bf16 v[66:69], v[222:225], v[206:209], v[66:69]
	s_setprio 0
	s_mov_b32 m0, s59
	s_barrier
	ds_read_b128 v[178:181], v152 offset:49152
	ds_read_b128 v[182:185], v152 offset:50176
	ds_read_b128 v[186:189], v152 offset:51200
	ds_read_b128 v[190:193], v152 offset:52224
	ds_read_b128 v[194:197], v152 offset:53248
	ds_read_b128 v[198:201], v152 offset:54272
	ds_read_b128 v[202:205], v152 offset:55296
	ds_read_b128 v[206:209], v152 offset:56320
	global_load_lds_dwordx4 v130, s[98:99]
	s_mov_b32 m0, s60
	s_nop 0
	global_load_lds_dwordx4 v134, s[98:99]
	s_barrier
	s_waitcnt lgkmcnt(0)
	s_setprio 1
	s_waitcnt lgkmcnt(0)
	v_mfma_f32_16x16x32_bf16 v[62:65], v[162:165], v[178:181], v[62:65]
	v_mfma_f32_16x16x32_bf16 v[58:61], v[170:173], v[178:181], v[58:61]
	v_mfma_f32_16x16x32_bf16 v[50:53], v[162:165], v[186:189], v[50:53]
	v_mfma_f32_16x16x32_bf16 v[42:45], v[170:173], v[186:189], v[42:45]
	v_mfma_f32_16x16x32_bf16 v[34:37], v[162:165], v[194:197], v[34:37]
	v_mfma_f32_16x16x32_bf16 v[26:29], v[170:173], v[194:197], v[26:29]
	v_mfma_f32_16x16x32_bf16 v[18:21], v[162:165], v[202:205], v[18:21]
	v_mfma_f32_16x16x32_bf16 v[10:13], v[170:173], v[202:205], v[10:13]
	v_mfma_f32_16x16x32_bf16 v[62:65], v[166:169], v[182:185], v[62:65]
	v_mfma_f32_16x16x32_bf16 v[58:61], v[174:177], v[182:185], v[58:61]
	v_mfma_f32_16x16x32_bf16 v[50:53], v[166:169], v[190:193], v[50:53]
	v_mfma_f32_16x16x32_bf16 v[42:45], v[174:177], v[190:193], v[42:45]
	v_mfma_f32_16x16x32_bf16 v[34:37], v[166:169], v[198:201], v[34:37]
	v_mfma_f32_16x16x32_bf16 v[26:29], v[174:177], v[198:201], v[26:29]
	v_mfma_f32_16x16x32_bf16 v[18:21], v[166:169], v[206:209], v[18:21]
	v_mfma_f32_16x16x32_bf16 v[10:13], v[174:177], v[206:209], v[10:13]
	s_setprio 0
	s_barrier
	s_add_u32 s40, s40, 0x100080
	s_addc_u32 s41, s41, 0
	s_add_i32 s42, s42, s54
	s_mov_b32 m0, s42
	s_nop 0
	global_load_lds_dwordx4 v132, s[40:41]
	s_add_i32 m0, s42, 0x2000
	s_nop 0
	global_load_lds_dwordx4 v136, s[40:41]
	s_waitcnt vmcnt(6)
	s_barrier
	s_setprio 1
	v_mfma_f32_16x16x32_bf16 v[54:57], v[210:213], v[178:181], v[54:57]
	v_mfma_f32_16x16x32_bf16 v[46:49], v[218:221], v[178:181], v[46:49]
	v_mfma_f32_16x16x32_bf16 v[38:41], v[210:213], v[186:189], v[38:41]
	v_mfma_f32_16x16x32_bf16 v[30:33], v[218:221], v[186:189], v[30:33]
	v_mfma_f32_16x16x32_bf16 v[22:25], v[210:213], v[194:197], v[22:25]
	v_mfma_f32_16x16x32_bf16 v[14:17], v[218:221], v[194:197], v[14:17]
	v_mfma_f32_16x16x32_bf16 v[6:9], v[210:213], v[202:205], v[6:9]
	v_mfma_f32_16x16x32_bf16 v[2:5], v[218:221], v[202:205], v[2:5]
	v_mfma_f32_16x16x32_bf16 v[54:57], v[214:217], v[182:185], v[54:57]
	v_mfma_f32_16x16x32_bf16 v[46:49], v[222:225], v[182:185], v[46:49]
	v_mfma_f32_16x16x32_bf16 v[38:41], v[214:217], v[190:193], v[38:41]
	v_mfma_f32_16x16x32_bf16 v[30:33], v[222:225], v[190:193], v[30:33]
	v_mfma_f32_16x16x32_bf16 v[22:25], v[214:217], v[198:201], v[22:25]
	v_mfma_f32_16x16x32_bf16 v[14:17], v[222:225], v[198:201], v[14:17]
	v_mfma_f32_16x16x32_bf16 v[6:9], v[214:217], v[206:209], v[6:9]
	v_mfma_f32_16x16x32_bf16 v[2:5], v[222:225], v[206:209], v[2:5]
	s_setprio 0
	s_add_i32 s71, s71, 2
	s_add_u32 s38, s38, 0x100
	s_addc_u32 s39, s39, 0
	s_add_u32 s69, s69, 0x100
	s_addc_u32 s70, s70, 0
	s_cmp_gt_u32 s71, 61
	s_barrier
	s_cbranch_scc0 .LBB0_1744
	s_and_b64 vcc, exec, s[14:15]
	s_cbranch_vccz .LBB0_1747
	s_barrier
